# write-through stores for every end-of-kernel output: last-tile epilogues of QKVG/GELU GEMMs and the split-K GEMM
# speedup vs baseline: 1.0104x; 1.0104x over previous
.LBB4_218:
	v_or_b32_e32 v130, s33, v161
	s_movk_i32 s14, 0x778
	v_mov_b32_e32 v8, s17
	v_ashrrev_i32_e32 v131, 31, v130
	v_bitop3_b32 v14, v160, s14, v8 bitop3:0xc8
	v_cvt_pk_f16_f32 v8, v120, v121
	v_lshlrev_b64 v[120:121], 12, v[130:131]
	v_mov_b32_e32 v129, 0
	v_lshl_add_u64 v[12:13], s[0:1], 0, v[120:121]
	v_lshlrev_b32_e32 v128, 1, v14
	v_cvt_pk_f16_f32 v11, v126, v127
	v_cvt_pk_f16_f32 v10, v124, v125
	v_cvt_pk_f16_f32 v9, v122, v123
	v_lshl_add_u64 v[12:13], v[12:13], 0, v[128:129]
	global_store_dwordx4 v[12:13], v[8:11], off sc1
	s_nop 1
	v_cndmask_b32_e64 v8, 0, 1, s[2:3]
	v_cmp_ne_u32_e64 s[0:1], 1, v8
	s_andn2_b64 vcc, exec, s[2:3]
	s_mov_b64 s[14:15], s[4:5]
	s_cbranch_vccnz .LBB4_228
	s_cmp_lt_i32 s18, 2
	s_cbranch_scc1 .LBB4_222
	s_cmp_eq_u32 s18, 2
	s_cbranch_scc0 .LBB4_223
	s_mov_b64 s[2:3], 0
	s_mov_b64 s[14:15], s[8:9]
	s_branch .LBB4_224

.LBB4_230:
	v_or_b32_e32 v12, 16, v130
	v_ashrrev_i32_e32 v13, 31, v12
	v_cvt_pk_f16_f32 v8, v112, v113
	v_lshlrev_b64 v[112:113], 12, v[12:13]
	v_lshl_add_u64 v[12:13], s[14:15], 0, v[112:113]
	v_mov_b32_e32 v129, 0
	v_cvt_pk_f16_f32 v11, v118, v119
	v_cvt_pk_f16_f32 v10, v116, v117
	v_cvt_pk_f16_f32 v9, v114, v115
	v_lshl_add_u64 v[12:13], v[12:13], 0, v[128:129]
	global_store_dwordx4 v[12:13], v[8:11], off sc1
	s_and_b64 vcc, exec, s[0:1]
	s_mov_b64 s[12:13], s[4:5]
	s_cbranch_vccnz .LBB4_240
	s_cmp_lt_i32 s18, 2
	s_cbranch_scc1 .LBB4_234
	s_cmp_eq_u32 s18, 2
	s_cbranch_scc0 .LBB4_235
	s_mov_b64 s[14:15], 0
	s_mov_b64 s[12:13], s[8:9]
	s_branch .LBB4_236

.LBB4_242:
	v_or_b32_e32 v12, 32, v130
	v_ashrrev_i32_e32 v13, 31, v12
	v_cvt_pk_f16_f32 v8, v104, v105
	v_lshlrev_b64 v[104:105], 12, v[12:13]
	v_lshl_add_u64 v[12:13], s[12:13], 0, v[104:105]
	v_mov_b32_e32 v129, 0
	v_cvt_pk_f16_f32 v11, v110, v111
	v_cvt_pk_f16_f32 v10, v108, v109
	v_cvt_pk_f16_f32 v9, v106, v107
	v_lshl_add_u64 v[12:13], v[12:13], 0, v[128:129]
	global_store_dwordx4 v[12:13], v[8:11], off sc1
	s_and_b64 vcc, exec, s[0:1]
	s_mov_b64 s[12:13], s[4:5]
	s_cbranch_vccnz .LBB4_252
	s_cmp_lt_i32 s18, 2
	s_cbranch_scc1 .LBB4_246
	s_cmp_eq_u32 s18, 2
	s_cbranch_scc0 .LBB4_247
	s_mov_b64 s[14:15], 0
	s_mov_b64 s[12:13], s[8:9]
	s_branch .LBB4_248

.LBB4_254:
	v_or_b32_e32 v12, 48, v130
	v_ashrrev_i32_e32 v13, 31, v12
	v_cvt_pk_f16_f32 v8, v96, v97
	v_lshlrev_b64 v[96:97], 12, v[12:13]
	v_lshl_add_u64 v[12:13], s[12:13], 0, v[96:97]
	v_mov_b32_e32 v129, 0
	v_cvt_pk_f16_f32 v11, v102, v103
	v_cvt_pk_f16_f32 v10, v100, v101
	v_cvt_pk_f16_f32 v9, v98, v99
	v_lshl_add_u64 v[12:13], v[12:13], 0, v[128:129]
	global_store_dwordx4 v[12:13], v[8:11], off sc1
	s_and_b64 vcc, exec, s[0:1]
	s_mov_b64 s[12:13], s[4:5]
	s_cbranch_vccnz .LBB4_264
	s_cmp_lt_i32 s18, 2
	s_cbranch_scc1 .LBB4_258
	s_cmp_eq_u32 s18, 2
	s_cbranch_scc0 .LBB4_259
	s_mov_b64 s[14:15], 0
	s_mov_b64 s[12:13], s[8:9]
	s_branch .LBB4_260

.LBB4_266:
	v_lshl_add_u64 v[12:13], s[12:13], 0, v[120:121]
	v_mov_b32_e32 v129, 0
	v_cvt_pk_f16_f32 v11, v94, v95
	v_cvt_pk_f16_f32 v10, v92, v93
	v_cvt_pk_f16_f32 v9, v90, v91
	v_cvt_pk_f16_f32 v8, v88, v89
	v_lshl_add_u64 v[12:13], v[12:13], 0, v[128:129]
	global_store_dwordx4 v[12:13], v[8:11], off offset:256 sc1
	s_and_b64 vcc, exec, s[0:1]
	s_mov_b64 s[12:13], s[4:5]
	s_cbranch_vccnz .LBB4_276
	s_cmp_lt_i32 s18, 2
	s_cbranch_scc1 .LBB4_270
	s_cmp_eq_u32 s18, 2
	s_cbranch_scc0 .LBB4_271
	s_mov_b64 s[14:15], 0
	s_mov_b64 s[12:13], s[8:9]
	s_branch .LBB4_272

.LBB4_278:
	v_lshl_add_u64 v[12:13], s[12:13], 0, v[112:113]
	v_mov_b32_e32 v129, 0
	v_cvt_pk_f16_f32 v11, v86, v87
	v_cvt_pk_f16_f32 v10, v84, v85
	v_cvt_pk_f16_f32 v9, v82, v83
	v_cvt_pk_f16_f32 v8, v80, v81
	v_lshl_add_u64 v[12:13], v[12:13], 0, v[128:129]
	global_store_dwordx4 v[12:13], v[8:11], off offset:256 sc1
	s_and_b64 vcc, exec, s[0:1]
	s_mov_b64 s[12:13], s[4:5]
	s_cbranch_vccnz .LBB4_288
	s_cmp_lt_i32 s18, 2
	s_cbranch_scc1 .LBB4_282
	s_cmp_eq_u32 s18, 2
	s_cbranch_scc0 .LBB4_283
	s_mov_b64 s[14:15], 0
	s_mov_b64 s[12:13], s[8:9]
	s_branch .LBB4_284

.LBB4_290:
	v_lshl_add_u64 v[12:13], s[12:13], 0, v[104:105]
	v_mov_b32_e32 v129, 0
	v_cvt_pk_f16_f32 v11, v78, v79
	v_cvt_pk_f16_f32 v10, v76, v77
	v_cvt_pk_f16_f32 v9, v74, v75
	v_cvt_pk_f16_f32 v8, v72, v73
	v_lshl_add_u64 v[12:13], v[12:13], 0, v[128:129]
	global_store_dwordx4 v[12:13], v[8:11], off offset:256 sc1
	s_and_b64 vcc, exec, s[0:1]
	s_mov_b64 s[12:13], s[4:5]
	s_cbranch_vccnz .LBB4_300
	s_cmp_lt_i32 s18, 2
	s_cbranch_scc1 .LBB4_294
	s_cmp_eq_u32 s18, 2
	s_cbranch_scc0 .LBB4_295
	s_mov_b64 s[14:15], 0
	s_mov_b64 s[12:13], s[8:9]
	s_branch .LBB4_296

.LBB4_302:
	v_lshl_add_u64 v[12:13], s[12:13], 0, v[96:97]
	v_mov_b32_e32 v129, 0
	v_cvt_pk_f16_f32 v11, v70, v71
	v_cvt_pk_f16_f32 v10, v68, v69
	v_cvt_pk_f16_f32 v9, v66, v67
	v_cvt_pk_f16_f32 v8, v64, v65
	v_lshl_add_u64 v[12:13], v[12:13], 0, v[128:129]
	global_store_dwordx4 v[12:13], v[8:11], off offset:256 sc1
	s_and_b64 vcc, exec, s[0:1]
	s_mov_b64 s[12:13], s[4:5]
	s_cbranch_vccnz .LBB4_312
	s_cmp_lt_i32 s18, 2
	s_cbranch_scc1 .LBB4_306
	s_cmp_eq_u32 s18, 2
	s_cbranch_scc0 .LBB4_307
	s_mov_b64 s[14:15], 0
	s_mov_b64 s[12:13], s[8:9]
	s_branch .LBB4_308

.LBB4_314:
	v_add_u32_e32 v64, s33, v254
	v_ashrrev_i32_e32 v65, 31, v64
	v_cvt_pk_f16_f32 v8, v56, v57
	v_lshlrev_b64 v[56:57], 12, v[64:65]
	v_lshl_add_u64 v[12:13], s[12:13], 0, v[56:57]
	v_mov_b32_e32 v129, 0
	v_cvt_pk_f16_f32 v11, v62, v63
	v_cvt_pk_f16_f32 v10, v60, v61
	v_cvt_pk_f16_f32 v9, v58, v59
	v_lshl_add_u64 v[12:13], v[12:13], 0, v[128:129]
	global_store_dwordx4 v[12:13], v[8:11], off sc1
	s_and_b64 vcc, exec, s[0:1]
	s_mov_b64 s[12:13], s[4:5]
	s_cbranch_vccnz .LBB4_324
	s_cmp_lt_i32 s18, 2
	s_cbranch_scc1 .LBB4_318
	s_cmp_eq_u32 s18, 2
	s_cbranch_scc0 .LBB4_319
	s_mov_b64 s[14:15], 0
	s_mov_b64 s[12:13], s[8:9]
	s_branch .LBB4_320

.LBB4_326:
	v_or_b32_e32 v12, 16, v64
	v_ashrrev_i32_e32 v13, 31, v12
	v_cvt_pk_f16_f32 v8, v48, v49
	v_lshlrev_b64 v[48:49], 12, v[12:13]
	v_lshl_add_u64 v[12:13], s[12:13], 0, v[48:49]
	v_mov_b32_e32 v129, 0
	v_cvt_pk_f16_f32 v11, v54, v55
	v_cvt_pk_f16_f32 v10, v52, v53
	v_cvt_pk_f16_f32 v9, v50, v51
	v_lshl_add_u64 v[12:13], v[12:13], 0, v[128:129]
	global_store_dwordx4 v[12:13], v[8:11], off sc1
	s_and_b64 vcc, exec, s[0:1]
	s_mov_b64 s[12:13], s[4:5]
	s_cbranch_vccnz .LBB4_336
	s_cmp_lt_i32 s18, 2
	s_cbranch_scc1 .LBB4_330
	s_cmp_eq_u32 s18, 2
	s_cbranch_scc0 .LBB4_331
	s_mov_b64 s[14:15], 0
	s_mov_b64 s[12:13], s[8:9]
	s_branch .LBB4_332

.LBB4_338:
	v_or_b32_e32 v12, 32, v64
	v_ashrrev_i32_e32 v13, 31, v12
	v_cvt_pk_f16_f32 v8, v40, v41
	v_lshlrev_b64 v[40:41], 12, v[12:13]
	v_lshl_add_u64 v[12:13], s[12:13], 0, v[40:41]
	v_mov_b32_e32 v129, 0
	v_cvt_pk_f16_f32 v11, v46, v47
	v_cvt_pk_f16_f32 v10, v44, v45
	v_cvt_pk_f16_f32 v9, v42, v43
	v_lshl_add_u64 v[12:13], v[12:13], 0, v[128:129]
	global_store_dwordx4 v[12:13], v[8:11], off sc1
	s_and_b64 vcc, exec, s[0:1]
	s_mov_b64 s[12:13], s[4:5]
	s_cbranch_vccnz .LBB4_348
	s_cmp_lt_i32 s18, 2
	s_cbranch_scc1 .LBB4_342
	s_cmp_eq_u32 s18, 2
	s_cbranch_scc0 .LBB4_343
	s_mov_b64 s[14:15], 0
	s_mov_b64 s[12:13], s[8:9]
	s_branch .LBB4_344

.LBB4_350:
	v_or_b32_e32 v12, 48, v64
	v_ashrrev_i32_e32 v13, 31, v12
	v_cvt_pk_f16_f32 v8, v32, v33
	v_lshlrev_b64 v[32:33], 12, v[12:13]
	v_lshl_add_u64 v[12:13], s[12:13], 0, v[32:33]
	v_mov_b32_e32 v129, 0
	v_cvt_pk_f16_f32 v11, v38, v39
	v_cvt_pk_f16_f32 v10, v36, v37
	v_cvt_pk_f16_f32 v9, v34, v35
	v_lshl_add_u64 v[12:13], v[12:13], 0, v[128:129]
	global_store_dwordx4 v[12:13], v[8:11], off sc1
	s_and_b64 vcc, exec, s[0:1]
	s_mov_b64 s[12:13], s[4:5]
	s_cbranch_vccnz .LBB4_360
	s_cmp_lt_i32 s18, 2
	s_cbranch_scc1 .LBB4_354
	s_cmp_eq_u32 s18, 2
	s_cbranch_scc0 .LBB4_355
	s_mov_b64 s[14:15], 0
	s_mov_b64 s[12:13], s[8:9]
	s_branch .LBB4_356

.LBB4_362:
	v_lshl_add_u64 v[12:13], s[12:13], 0, v[56:57]
	v_mov_b32_e32 v129, 0
	v_cvt_pk_f16_f32 v11, v30, v31
	v_cvt_pk_f16_f32 v10, v28, v29
	v_cvt_pk_f16_f32 v9, v26, v27
	v_cvt_pk_f16_f32 v8, v24, v25
	v_lshl_add_u64 v[12:13], v[12:13], 0, v[128:129]
	global_store_dwordx4 v[12:13], v[8:11], off offset:256 sc1
	s_and_b64 vcc, exec, s[0:1]
	s_mov_b64 s[12:13], s[4:5]
	s_cbranch_vccnz .LBB4_372
	s_cmp_lt_i32 s18, 2
	s_cbranch_scc1 .LBB4_366
	s_cmp_eq_u32 s18, 2
	s_cbranch_scc0 .LBB4_367
	s_mov_b64 s[14:15], 0
	s_mov_b64 s[12:13], s[8:9]
	s_branch .LBB4_368

.LBB4_374:
	v_lshl_add_u64 v[12:13], s[12:13], 0, v[48:49]
	v_mov_b32_e32 v129, 0
	v_cvt_pk_f16_f32 v11, v22, v23
	v_cvt_pk_f16_f32 v10, v20, v21
	v_cvt_pk_f16_f32 v9, v18, v19
	v_cvt_pk_f16_f32 v8, v16, v17
	v_lshl_add_u64 v[12:13], v[12:13], 0, v[128:129]
	global_store_dwordx4 v[12:13], v[8:11], off offset:256 sc1
	s_and_b64 vcc, exec, s[0:1]
	s_mov_b64 s[12:13], s[4:5]
	s_cbranch_vccnz .LBB4_384
	s_cmp_lt_i32 s18, 2
	s_cbranch_scc1 .LBB4_378
	s_cmp_eq_u32 s18, 2
	s_cbranch_scc0 .LBB4_379
	s_mov_b64 s[14:15], 0
	s_mov_b64 s[12:13], s[8:9]
	s_branch .LBB4_380

.LBB4_386:
	v_lshl_add_u64 v[12:13], s[12:13], 0, v[40:41]
	v_mov_b32_e32 v129, 0
	v_cvt_pk_f16_f32 v11, v140, v141
	v_cvt_pk_f16_f32 v10, v138, v139
	v_cvt_pk_f16_f32 v9, v136, v137
	v_cvt_pk_f16_f32 v8, v134, v135
	v_lshl_add_u64 v[12:13], v[12:13], 0, v[128:129]
	global_store_dwordx4 v[12:13], v[8:11], off offset:256 sc1
	s_and_b64 vcc, exec, s[0:1]
	s_cbranch_vccnz .LBB4_396
	s_cmp_lt_i32 s18, 2
	s_cbranch_scc1 .LBB4_390
	s_cmp_eq_u32 s18, 2
	s_cbranch_scc0 .LBB4_391
	s_mov_b64 s[0:1], 0
	s_mov_b64 s[4:5], s[8:9]
	s_branch .LBB4_392

.LBB4_398:
	v_cvt_pk_f16_f32 v7, v6, v7
	v_cvt_pk_f16_f32 v6, v4, v5
	v_cvt_pk_f16_f32 v4, v0, v1
	v_lshl_add_u64 v[0:1], s[4:5], 0, v[32:33]
	v_mov_b32_e32 v129, 0
	v_cvt_pk_f16_f32 v5, v2, v3
	v_lshl_add_u64 v[0:1], v[0:1], 0, v[128:129]
	global_store_dwordx4 v[0:1], v[4:7], off offset:256 sc1
	s_endpgm
	.p2align	8

.LBB5_15:
	s_or_b64 exec, exec, s[2:3]
	s_ashr_i32 s13, s12, 31
	s_lshl_b64 s[2:3], s[12:13], 24
	v_lshlrev_b32_e32 v129, 5, v144
	s_add_u32 s0, s0, s2
	v_or3_b32 v130, v129, v142, s8
	v_or3_b32 v132, v143, v145, s9
	s_addc_u32 s1, s1, s3
	v_ashrrev_i32_e32 v131, 31, v130
	v_ashrrev_i32_e32 v133, 31, v132
	v_lshl_add_u64 v[130:131], v[130:131], 1, s[0:1]
	v_cvt_pk_f16_f32 v127, v126, v127
	v_cvt_pk_f16_f32 v126, v124, v125
	v_cvt_pk_f16_f32 v124, v120, v121
	v_lshlrev_b64 v[120:121], 12, v[132:133]
	v_or_b32_e32 v128, s6, v143
	v_cvt_pk_f16_f32 v125, v122, v123
	v_lshl_add_u64 v[120:121], v[130:131], 0, v[120:121]
	v_add_u32_e32 v128, v145, v128
	global_store_dwordx4 v[120:121], v[124:127], off sc1
	v_or_b32_e32 v122, 16, v132
	v_ashrrev_i32_e32 v123, 31, v122
	v_cvt_pk_f16_f32 v119, v118, v119
	v_cvt_pk_f16_f32 v118, v116, v117
	v_cvt_pk_f16_f32 v116, v112, v113
	v_lshlrev_b64 v[112:113], 12, v[122:123]
	v_cvt_pk_f16_f32 v117, v114, v115
	v_lshl_add_u64 v[112:113], v[130:131], 0, v[112:113]
	global_store_dwordx4 v[112:113], v[116:119], off sc1
	v_or_b32_e32 v114, 32, v132
	v_ashrrev_i32_e32 v115, 31, v114
	v_cvt_pk_f16_f32 v111, v110, v111
	v_cvt_pk_f16_f32 v110, v108, v109
	v_cvt_pk_f16_f32 v108, v104, v105
	v_lshlrev_b64 v[104:105], 12, v[114:115]
	v_cvt_pk_f16_f32 v109, v106, v107
	v_lshl_add_u64 v[104:105], v[130:131], 0, v[104:105]
	global_store_dwordx4 v[104:105], v[108:111], off sc1
	v_or_b32_e32 v106, 48, v132
	v_ashrrev_i32_e32 v107, 31, v106
	v_cvt_pk_f16_f32 v95, v94, v95
	v_cvt_pk_f16_f32 v94, v92, v93
	v_cvt_pk_f16_f32 v92, v84, v85
	v_lshlrev_b64 v[84:85], 12, v[106:107]
	v_cvt_pk_f16_f32 v93, v86, v87
	v_lshl_add_u64 v[106:107], v[130:131], 0, v[84:85]
	global_store_dwordx4 v[106:107], v[92:95], off sc1
	v_cvt_pk_f16_f32 v87, v102, v103
	v_cvt_pk_f16_f32 v86, v100, v101
	v_cvt_pk_f16_f32 v85, v98, v99
	v_cvt_pk_f16_f32 v84, v96, v97
	global_store_dwordx4 v[120:121], v[84:87], off offset:256 sc1
	s_nop 1
	v_cvt_pk_f16_f32 v85, v90, v91
	v_cvt_pk_f16_f32 v84, v88, v89
	v_cvt_pk_f16_f32 v83, v82, v83
	v_cvt_pk_f16_f32 v82, v80, v81
	global_store_dwordx4 v[112:113], v[82:85], off offset:256 sc1
	v_cvt_pk_f16_f32 v75, v74, v75
	v_cvt_pk_f16_f32 v74, v72, v73
	v_cvt_pk_f16_f32 v73, v66, v67
	v_cvt_pk_f16_f32 v72, v64, v65
	global_store_dwordx4 v[104:105], v[72:75], off offset:256 sc1
	v_cvt_pk_f16_f32 v63, v62, v63
	v_cvt_pk_f16_f32 v62, v60, v61
	v_cvt_pk_f16_f32 v61, v58, v59
	v_cvt_pk_f16_f32 v60, v56, v57
	global_store_dwordx4 v[106:107], v[60:63], off offset:256 sc1
	v_ashrrev_i32_e32 v129, 31, v128
	s_nop 0
	v_lshlrev_b64 v[60:61], 12, v[128:129]
	v_cvt_pk_f16_f32 v59, v78, v79
	v_cvt_pk_f16_f32 v58, v76, v77
	v_cvt_pk_f16_f32 v57, v70, v71
	v_cvt_pk_f16_f32 v56, v68, v69
	v_lshl_add_u64 v[60:61], v[130:131], 0, v[60:61]
	global_store_dwordx4 v[60:61], v[56:59], off sc1
	s_nop 1
	v_or_b32_e32 v56, 16, v128
	v_ashrrev_i32_e32 v57, 31, v56
	v_cvt_pk_f16_f32 v55, v54, v55
	v_cvt_pk_f16_f32 v54, v52, v53
	v_cvt_pk_f16_f32 v52, v48, v49
	v_lshlrev_b64 v[48:49], 12, v[56:57]
	v_cvt_pk_f16_f32 v53, v50, v51
	v_lshl_add_u64 v[48:49], v[130:131], 0, v[48:49]
	global_store_dwordx4 v[48:49], v[52:55], off sc1
	v_or_b32_e32 v50, 32, v128
	v_ashrrev_i32_e32 v51, 31, v50
	v_cvt_pk_f16_f32 v47, v46, v47
	v_cvt_pk_f16_f32 v46, v44, v45
	v_cvt_pk_f16_f32 v44, v40, v41
	v_lshlrev_b64 v[40:41], 12, v[50:51]
	v_cvt_pk_f16_f32 v45, v42, v43
	v_lshl_add_u64 v[40:41], v[130:131], 0, v[40:41]
	global_store_dwordx4 v[40:41], v[44:47], off sc1
	v_or_b32_e32 v42, 48, v128
	v_ashrrev_i32_e32 v43, 31, v42
	v_cvt_pk_f16_f32 v39, v38, v39
	v_cvt_pk_f16_f32 v38, v36, v37
	v_cvt_pk_f16_f32 v36, v32, v33
	v_lshlrev_b64 v[32:33], 12, v[42:43]
	v_cvt_pk_f16_f32 v37, v34, v35
	v_lshl_add_u64 v[32:33], v[130:131], 0, v[32:33]
	global_store_dwordx4 v[32:33], v[36:39], off sc1
	v_cvt_pk_f16_f32 v31, v30, v31
	v_cvt_pk_f16_f32 v30, v28, v29
	v_cvt_pk_f16_f32 v29, v26, v27
	v_cvt_pk_f16_f32 v28, v24, v25
	global_store_dwordx4 v[60:61], v[28:31], off offset:256 sc1
	v_cvt_pk_f16_f32 v23, v22, v23
	v_cvt_pk_f16_f32 v22, v20, v21
	v_cvt_pk_f16_f32 v21, v18, v19
	v_cvt_pk_f16_f32 v20, v16, v17
	global_store_dwordx4 v[48:49], v[20:23], off offset:256 sc1
	v_cvt_pk_f16_f32 v15, v14, v15
	v_cvt_pk_f16_f32 v14, v12, v13
	v_cvt_pk_f16_f32 v13, v10, v11
	v_cvt_pk_f16_f32 v12, v8, v9
	global_store_dwordx4 v[40:41], v[12:15], off offset:256 sc1
	v_cvt_pk_f16_f32 v7, v6, v7
	v_cvt_pk_f16_f32 v6, v4, v5
	v_cvt_pk_f16_f32 v5, v2, v3
	v_cvt_pk_f16_f32 v4, v0, v1
	global_store_dwordx4 v[32:33], v[4:7], off offset:256 sc1
	s_endpgm
	.p2align	8

.LBB7_14:
	s_or_b64 exec, exec, s[0:1]
	v_or_b32_e32 v146, s23, v168
	v_ashrrev_i32_e32 v147, 31, v146
	v_lshl_add_u64 v[12:13], v[146:147], 2, s[12:13]
	global_load_dwordx4 v[52:55], v[12:13], off
	global_load_dwordx4 v[48:51], v[12:13], off offset:16
	global_load_dwordx4 v[8:11], v[12:13], off offset:528
	s_nop 0
	global_load_dwordx4 v[12:15], v[12:13], off offset:512
	s_mov_b32 s2, 0xc0135761
	s_mov_b32 s0, 0x3dd2d3e8
	v_mov_b64_e32 v[144:145], s[2:3]
	v_or_b32_e32 v148, s11, v167
	v_ashrrev_i32_e32 v149, 31, v148
	v_lshl_add_u64 v[146:147], v[146:147], 1, s[8:9]
	v_lshlrev_b64 v[150:151], 14, v[148:149]
	s_waitcnt vmcnt(0)
	v_pk_add_f32 v[138:139], v[138:139], v[54:55]
	v_pk_add_f32 v[136:137], v[136:137], v[52:53]
	v_pk_add_f32 v[142:143], v[142:143], v[50:51]
	v_pk_add_f32 v[140:141], v[140:141], v[48:49]
	v_pk_mul_f32 v[152:153], v[138:139], v[138:139]
	v_pk_mul_f32 v[154:155], v[136:137], v[136:137]
	v_pk_mul_f32 v[156:157], v[142:143], v[142:143]
	v_pk_mul_f32 v[158:159], v[140:141], v[140:141]
	v_pk_fma_f32 v[154:155], v[154:155], s[0:1], v[144:145] op_sel_hi:[1,0,0] neg_lo:[1,0,0] neg_hi:[1,0,0]
	v_pk_fma_f32 v[152:153], v[152:153], s[0:1], v[144:145] op_sel_hi:[1,0,0] neg_lo:[1,0,0] neg_hi:[1,0,0]
	v_pk_fma_f32 v[158:159], v[158:159], s[0:1], v[144:145] op_sel_hi:[1,0,0] neg_lo:[1,0,0] neg_hi:[1,0,0]
	v_pk_fma_f32 v[156:157], v[156:157], s[0:1], v[144:145] op_sel_hi:[1,0,0] neg_lo:[1,0,0] neg_hi:[1,0,0]
	v_pk_mul_f32 v[154:155], v[136:137], v[154:155]
	v_pk_mul_f32 v[152:153], v[138:139], v[152:153]
	v_pk_mul_f32 v[158:159], v[140:141], v[158:159]
	v_pk_mul_f32 v[156:157], v[142:143], v[156:157]
	v_exp_f32_e32 v154, v154
	v_exp_f32_e32 v155, v155
	v_exp_f32_e32 v152, v152
	v_exp_f32_e32 v153, v153
	v_exp_f32_e32 v158, v158
	v_exp_f32_e32 v159, v159
	v_exp_f32_e32 v156, v156
	v_exp_f32_e32 v157, v157
	v_pk_add_f32 v[154:155], v[154:155], 1.0 op_sel_hi:[1,0]
	v_pk_add_f32 v[152:153], v[152:153], 1.0 op_sel_hi:[1,0]
	v_pk_add_f32 v[158:159], v[158:159], 1.0 op_sel_hi:[1,0]
	v_pk_add_f32 v[156:157], v[156:157], 1.0 op_sel_hi:[1,0]
	v_rcp_f32_e32 v154, v154
	v_rcp_f32_e32 v155, v155
	v_rcp_f32_e32 v152, v152
	v_rcp_f32_e32 v153, v153
	v_rcp_f32_e32 v158, v158
	v_rcp_f32_e32 v159, v159
	v_rcp_f32_e32 v156, v156
	v_rcp_f32_e32 v157, v157
	v_pk_mul_f32 v[136:137], v[136:137], v[154:155]
	v_pk_mul_f32 v[138:139], v[138:139], v[152:153]
	v_pk_mul_f32 v[152:153], v[140:141], v[158:159]
	v_pk_mul_f32 v[140:141], v[142:143], v[156:157]
	v_cvt_pk_f16_f32 v139, v138, v139
	v_cvt_pk_f16_f32 v141, v140, v141
	v_cvt_pk_f16_f32 v140, v152, v153
	v_cvt_pk_f16_f32 v138, v136, v137
	v_lshl_add_u64 v[136:137], v[146:147], 0, v[150:151]
	global_store_dwordx4 v[136:137], v[138:141], off sc1
	v_pk_add_f32 v[128:129], v[128:129], v[48:49]
	v_pk_add_f32 v[134:135], v[134:135], v[54:55]
	v_pk_add_f32 v[132:133], v[132:133], v[52:53]
	v_pk_add_f32 v[130:131], v[130:131], v[50:51]
	v_pk_mul_f32 v[152:153], v[128:129], v[128:129]
	v_pk_mul_f32 v[140:141], v[134:135], v[134:135]
	v_pk_mul_f32 v[142:143], v[132:133], v[132:133]
	v_pk_mul_f32 v[150:151], v[130:131], v[130:131]
	v_pk_fma_f32 v[152:153], v[152:153], s[0:1], v[144:145] op_sel_hi:[1,0,0] neg_lo:[1,0,0] neg_hi:[1,0,0]
	v_pk_fma_f32 v[142:143], v[142:143], s[0:1], v[144:145] op_sel_hi:[1,0,0] neg_lo:[1,0,0] neg_hi:[1,0,0]
	v_pk_fma_f32 v[140:141], v[140:141], s[0:1], v[144:145] op_sel_hi:[1,0,0] neg_lo:[1,0,0] neg_hi:[1,0,0]
	v_pk_mul_f32 v[152:153], v[128:129], v[152:153]
	v_pk_fma_f32 v[150:151], v[150:151], s[0:1], v[144:145] op_sel_hi:[1,0,0] neg_lo:[1,0,0] neg_hi:[1,0,0]
	v_pk_mul_f32 v[142:143], v[132:133], v[142:143]
	v_pk_mul_f32 v[140:141], v[134:135], v[140:141]
	v_exp_f32_e32 v152, v152
	v_exp_f32_e32 v153, v153
	v_pk_mul_f32 v[150:151], v[130:131], v[150:151]
	v_exp_f32_e32 v142, v142
	v_exp_f32_e32 v143, v143
	v_exp_f32_e32 v140, v140
	v_exp_f32_e32 v141, v141
	v_exp_f32_e32 v150, v150
	v_exp_f32_e32 v151, v151
	v_pk_add_f32 v[152:153], v[152:153], 1.0 op_sel_hi:[1,0]
	v_pk_add_f32 v[142:143], v[142:143], 1.0 op_sel_hi:[1,0]
	v_pk_add_f32 v[140:141], v[140:141], 1.0 op_sel_hi:[1,0]
	v_rcp_f32_e32 v152, v152
	v_rcp_f32_e32 v153, v153
	v_pk_add_f32 v[150:151], v[150:151], 1.0 op_sel_hi:[1,0]
	v_rcp_f32_e32 v142, v142
	v_rcp_f32_e32 v143, v143
	v_rcp_f32_e32 v140, v140
	v_rcp_f32_e32 v141, v141
	v_rcp_f32_e32 v150, v150
	v_rcp_f32_e32 v151, v151
	v_or_b32_e32 v138, 16, v148
	v_pk_mul_f32 v[128:129], v[128:129], v[152:153]
	v_ashrrev_i32_e32 v139, 31, v138
	v_pk_mul_f32 v[142:143], v[132:133], v[142:143]
	v_pk_mul_f32 v[134:135], v[134:135], v[140:141]
	v_pk_mul_f32 v[130:131], v[130:131], v[150:151]
	v_cvt_pk_f16_f32 v132, v128, v129
	v_lshlrev_b64 v[128:129], 14, v[138:139]
	v_cvt_pk_f16_f32 v133, v130, v131
	v_cvt_pk_f16_f32 v131, v134, v135
	v_cvt_pk_f16_f32 v130, v142, v143
	v_lshl_add_u64 v[128:129], v[146:147], 0, v[128:129]
	global_store_dwordx4 v[128:129], v[130:133], off sc1
	v_pk_add_f32 v[120:121], v[120:121], v[48:49]
	v_pk_add_f32 v[126:127], v[126:127], v[54:55]
	v_pk_add_f32 v[124:125], v[124:125], v[52:53]
	v_pk_add_f32 v[122:123], v[122:123], v[50:51]
	v_pk_mul_f32 v[140:141], v[120:121], v[120:121]
	v_pk_mul_f32 v[132:133], v[126:127], v[126:127]
	v_pk_mul_f32 v[134:135], v[124:125], v[124:125]
	v_pk_mul_f32 v[138:139], v[122:123], v[122:123]
	v_pk_fma_f32 v[140:141], v[140:141], s[0:1], v[144:145] op_sel_hi:[1,0,0] neg_lo:[1,0,0] neg_hi:[1,0,0]
	v_pk_fma_f32 v[134:135], v[134:135], s[0:1], v[144:145] op_sel_hi:[1,0,0] neg_lo:[1,0,0] neg_hi:[1,0,0]
	v_pk_fma_f32 v[132:133], v[132:133], s[0:1], v[144:145] op_sel_hi:[1,0,0] neg_lo:[1,0,0] neg_hi:[1,0,0]
	v_pk_mul_f32 v[140:141], v[120:121], v[140:141]
	v_pk_fma_f32 v[138:139], v[138:139], s[0:1], v[144:145] op_sel_hi:[1,0,0] neg_lo:[1,0,0] neg_hi:[1,0,0]
	v_pk_mul_f32 v[134:135], v[124:125], v[134:135]
	v_pk_mul_f32 v[132:133], v[126:127], v[132:133]
	v_exp_f32_e32 v140, v140
	v_exp_f32_e32 v141, v141
	v_pk_mul_f32 v[138:139], v[122:123], v[138:139]
	v_exp_f32_e32 v134, v134
	v_exp_f32_e32 v135, v135
	v_exp_f32_e32 v132, v132
	v_exp_f32_e32 v133, v133
	v_exp_f32_e32 v138, v138
	v_exp_f32_e32 v139, v139
	v_pk_add_f32 v[140:141], v[140:141], 1.0 op_sel_hi:[1,0]
	v_pk_add_f32 v[134:135], v[134:135], 1.0 op_sel_hi:[1,0]
	v_pk_add_f32 v[132:133], v[132:133], 1.0 op_sel_hi:[1,0]
	v_rcp_f32_e32 v140, v140
	v_rcp_f32_e32 v141, v141
	v_pk_add_f32 v[138:139], v[138:139], 1.0 op_sel_hi:[1,0]
	v_rcp_f32_e32 v134, v134
	v_rcp_f32_e32 v135, v135
	v_rcp_f32_e32 v132, v132
	v_rcp_f32_e32 v133, v133
	v_rcp_f32_e32 v138, v138
	v_rcp_f32_e32 v139, v139
	v_or_b32_e32 v130, 32, v148
	v_pk_mul_f32 v[120:121], v[120:121], v[140:141]
	v_ashrrev_i32_e32 v131, 31, v130
	v_pk_mul_f32 v[134:135], v[124:125], v[134:135]
	v_pk_mul_f32 v[126:127], v[126:127], v[132:133]
	v_pk_mul_f32 v[122:123], v[122:123], v[138:139]
	v_cvt_pk_f16_f32 v124, v120, v121
	v_lshlrev_b64 v[120:121], 14, v[130:131]
	v_cvt_pk_f16_f32 v125, v122, v123
	v_cvt_pk_f16_f32 v123, v126, v127
	v_cvt_pk_f16_f32 v122, v134, v135
	v_lshl_add_u64 v[120:121], v[146:147], 0, v[120:121]
	global_store_dwordx4 v[120:121], v[122:125], off sc1
	v_pk_add_f32 v[112:113], v[112:113], v[48:49]
	v_pk_add_f32 v[118:119], v[118:119], v[54:55]
	v_pk_add_f32 v[116:117], v[116:117], v[52:53]
	v_pk_add_f32 v[114:115], v[114:115], v[50:51]
	v_pk_mul_f32 v[132:133], v[112:113], v[112:113]
	v_pk_mul_f32 v[124:125], v[118:119], v[118:119]
	v_pk_mul_f32 v[126:127], v[116:117], v[116:117]
	v_pk_mul_f32 v[130:131], v[114:115], v[114:115]
	v_pk_fma_f32 v[132:133], v[132:133], s[0:1], v[144:145] op_sel_hi:[1,0,0] neg_lo:[1,0,0] neg_hi:[1,0,0]
	v_pk_fma_f32 v[126:127], v[126:127], s[0:1], v[144:145] op_sel_hi:[1,0,0] neg_lo:[1,0,0] neg_hi:[1,0,0]
	v_pk_fma_f32 v[124:125], v[124:125], s[0:1], v[144:145] op_sel_hi:[1,0,0] neg_lo:[1,0,0] neg_hi:[1,0,0]
	v_pk_mul_f32 v[132:133], v[112:113], v[132:133]
	v_pk_fma_f32 v[130:131], v[130:131], s[0:1], v[144:145] op_sel_hi:[1,0,0] neg_lo:[1,0,0] neg_hi:[1,0,0]
	v_pk_mul_f32 v[126:127], v[116:117], v[126:127]
	v_pk_mul_f32 v[124:125], v[118:119], v[124:125]
	v_exp_f32_e32 v132, v132
	v_exp_f32_e32 v133, v133
	v_pk_mul_f32 v[130:131], v[114:115], v[130:131]
	v_exp_f32_e32 v126, v126
	v_exp_f32_e32 v127, v127
	v_exp_f32_e32 v124, v124
	v_exp_f32_e32 v125, v125
	v_exp_f32_e32 v130, v130
	v_exp_f32_e32 v131, v131
	v_pk_add_f32 v[132:133], v[132:133], 1.0 op_sel_hi:[1,0]
	v_pk_add_f32 v[126:127], v[126:127], 1.0 op_sel_hi:[1,0]
	v_pk_add_f32 v[124:125], v[124:125], 1.0 op_sel_hi:[1,0]
	v_rcp_f32_e32 v132, v132
	v_rcp_f32_e32 v133, v133
	v_pk_add_f32 v[130:131], v[130:131], 1.0 op_sel_hi:[1,0]
	v_rcp_f32_e32 v126, v126
	v_rcp_f32_e32 v127, v127
	v_rcp_f32_e32 v124, v124
	v_rcp_f32_e32 v125, v125
	v_rcp_f32_e32 v130, v130
	v_rcp_f32_e32 v131, v131
	v_or_b32_e32 v122, 48, v148
	v_pk_mul_f32 v[112:113], v[112:113], v[132:133]
	v_ashrrev_i32_e32 v123, 31, v122
	v_pk_mul_f32 v[126:127], v[116:117], v[126:127]
	v_pk_mul_f32 v[118:119], v[118:119], v[124:125]
	v_pk_mul_f32 v[114:115], v[114:115], v[130:131]
	v_cvt_pk_f16_f32 v116, v112, v113
	v_lshlrev_b64 v[112:113], 14, v[122:123]
	v_cvt_pk_f16_f32 v117, v114, v115
	v_cvt_pk_f16_f32 v115, v118, v119
	v_cvt_pk_f16_f32 v114, v126, v127
	v_lshl_add_u64 v[112:113], v[146:147], 0, v[112:113]
	global_store_dwordx4 v[112:113], v[114:117], off sc1
	v_pk_add_f32 v[110:111], v[110:111], v[14:15]
	v_pk_add_f32 v[108:109], v[108:109], v[12:13]
	v_pk_add_f32 v[106:107], v[106:107], v[10:11]
	v_pk_add_f32 v[104:105], v[104:105], v[8:9]
	v_pk_mul_f32 v[114:115], v[110:111], v[110:111]
	v_pk_mul_f32 v[116:117], v[108:109], v[108:109]
	v_pk_mul_f32 v[118:119], v[106:107], v[106:107]
	v_pk_mul_f32 v[122:123], v[104:105], v[104:105]
	v_pk_fma_f32 v[116:117], v[116:117], s[0:1], v[144:145] op_sel_hi:[1,0,0] neg_lo:[1,0,0] neg_hi:[1,0,0]
	v_pk_fma_f32 v[114:115], v[114:115], s[0:1], v[144:145] op_sel_hi:[1,0,0] neg_lo:[1,0,0] neg_hi:[1,0,0]
	v_pk_fma_f32 v[122:123], v[122:123], s[0:1], v[144:145] op_sel_hi:[1,0,0] neg_lo:[1,0,0] neg_hi:[1,0,0]
	v_pk_fma_f32 v[118:119], v[118:119], s[0:1], v[144:145] op_sel_hi:[1,0,0] neg_lo:[1,0,0] neg_hi:[1,0,0]
	v_pk_mul_f32 v[116:117], v[108:109], v[116:117]
	v_pk_mul_f32 v[114:115], v[110:111], v[114:115]
	v_pk_mul_f32 v[122:123], v[104:105], v[122:123]
	v_pk_mul_f32 v[118:119], v[106:107], v[118:119]
	v_exp_f32_e32 v116, v116
	v_exp_f32_e32 v117, v117
	v_exp_f32_e32 v114, v114
	v_exp_f32_e32 v115, v115
	v_exp_f32_e32 v122, v122
	v_exp_f32_e32 v123, v123
	v_exp_f32_e32 v118, v118
	v_exp_f32_e32 v119, v119
	v_pk_add_f32 v[116:117], v[116:117], 1.0 op_sel_hi:[1,0]
	v_pk_add_f32 v[114:115], v[114:115], 1.0 op_sel_hi:[1,0]
	v_pk_add_f32 v[122:123], v[122:123], 1.0 op_sel_hi:[1,0]
	v_pk_add_f32 v[118:119], v[118:119], 1.0 op_sel_hi:[1,0]
	v_rcp_f32_e32 v116, v116
	v_rcp_f32_e32 v117, v117
	v_rcp_f32_e32 v114, v114
	v_rcp_f32_e32 v115, v115
	v_rcp_f32_e32 v122, v122
	v_rcp_f32_e32 v123, v123
	v_rcp_f32_e32 v118, v118
	v_rcp_f32_e32 v119, v119
	v_pk_mul_f32 v[108:109], v[108:109], v[116:117]
	v_pk_mul_f32 v[110:111], v[110:111], v[114:115]
	v_pk_mul_f32 v[114:115], v[104:105], v[122:123]
	v_pk_mul_f32 v[104:105], v[106:107], v[118:119]
	v_cvt_pk_f16_f32 v106, v114, v115
	v_cvt_pk_f16_f32 v107, v104, v105
	v_cvt_pk_f16_f32 v105, v110, v111
	v_cvt_pk_f16_f32 v104, v108, v109
	global_store_dwordx4 v[136:137], v[104:107], off offset:256 sc1
	v_pk_add_f32 v[102:103], v[102:103], v[14:15]
	v_pk_add_f32 v[100:101], v[100:101], v[12:13]
	v_pk_add_f32 v[98:99], v[98:99], v[10:11]
	v_pk_add_f32 v[96:97], v[96:97], v[8:9]
	v_pk_mul_f32 v[104:105], v[102:103], v[102:103]
	v_pk_mul_f32 v[106:107], v[100:101], v[100:101]
	v_pk_mul_f32 v[108:109], v[98:99], v[98:99]
	v_pk_mul_f32 v[110:111], v[96:97], v[96:97]
	v_pk_fma_f32 v[106:107], v[106:107], s[0:1], v[144:145] op_sel_hi:[1,0,0] neg_lo:[1,0,0] neg_hi:[1,0,0]
	v_pk_fma_f32 v[104:105], v[104:105], s[0:1], v[144:145] op_sel_hi:[1,0,0] neg_lo:[1,0,0] neg_hi:[1,0,0]
	v_pk_fma_f32 v[110:111], v[110:111], s[0:1], v[144:145] op_sel_hi:[1,0,0] neg_lo:[1,0,0] neg_hi:[1,0,0]
	v_pk_fma_f32 v[108:109], v[108:109], s[0:1], v[144:145] op_sel_hi:[1,0,0] neg_lo:[1,0,0] neg_hi:[1,0,0]
	v_pk_mul_f32 v[106:107], v[100:101], v[106:107]
	v_pk_mul_f32 v[104:105], v[102:103], v[104:105]
	v_pk_mul_f32 v[110:111], v[96:97], v[110:111]
	v_pk_mul_f32 v[108:109], v[98:99], v[108:109]
	v_exp_f32_e32 v106, v106
	v_exp_f32_e32 v107, v107
	v_exp_f32_e32 v104, v104
	v_exp_f32_e32 v105, v105
	v_exp_f32_e32 v110, v110
	v_exp_f32_e32 v111, v111
	v_exp_f32_e32 v108, v108
	v_exp_f32_e32 v109, v109
	v_pk_add_f32 v[106:107], v[106:107], 1.0 op_sel_hi:[1,0]
	v_pk_add_f32 v[104:105], v[104:105], 1.0 op_sel_hi:[1,0]
	v_pk_add_f32 v[110:111], v[110:111], 1.0 op_sel_hi:[1,0]
	v_pk_add_f32 v[108:109], v[108:109], 1.0 op_sel_hi:[1,0]
	v_rcp_f32_e32 v106, v106
	v_rcp_f32_e32 v107, v107
	v_rcp_f32_e32 v104, v104
	v_rcp_f32_e32 v105, v105
	v_rcp_f32_e32 v110, v110
	v_rcp_f32_e32 v111, v111
	v_rcp_f32_e32 v108, v108
	v_rcp_f32_e32 v109, v109
	v_pk_mul_f32 v[100:101], v[100:101], v[106:107]
	v_pk_mul_f32 v[102:103], v[102:103], v[104:105]
	v_pk_mul_f32 v[104:105], v[96:97], v[110:111]
	v_pk_mul_f32 v[96:97], v[98:99], v[108:109]
	v_cvt_pk_f16_f32 v98, v104, v105
	v_cvt_pk_f16_f32 v99, v96, v97
	v_cvt_pk_f16_f32 v97, v102, v103
	v_cvt_pk_f16_f32 v96, v100, v101
	global_store_dwordx4 v[128:129], v[96:99], off offset:256 sc1
	v_pk_add_f32 v[94:95], v[94:95], v[14:15]
	v_pk_add_f32 v[92:93], v[92:93], v[12:13]
	v_pk_add_f32 v[90:91], v[90:91], v[10:11]
	v_pk_add_f32 v[88:89], v[88:89], v[8:9]
	v_pk_mul_f32 v[96:97], v[94:95], v[94:95]
	v_pk_mul_f32 v[98:99], v[92:93], v[92:93]
	v_pk_mul_f32 v[100:101], v[90:91], v[90:91]
	v_pk_mul_f32 v[102:103], v[88:89], v[88:89]
	v_pk_fma_f32 v[98:99], v[98:99], s[0:1], v[144:145] op_sel_hi:[1,0,0] neg_lo:[1,0,0] neg_hi:[1,0,0]
	v_pk_fma_f32 v[96:97], v[96:97], s[0:1], v[144:145] op_sel_hi:[1,0,0] neg_lo:[1,0,0] neg_hi:[1,0,0]
	v_pk_fma_f32 v[102:103], v[102:103], s[0:1], v[144:145] op_sel_hi:[1,0,0] neg_lo:[1,0,0] neg_hi:[1,0,0]
	v_pk_fma_f32 v[100:101], v[100:101], s[0:1], v[144:145] op_sel_hi:[1,0,0] neg_lo:[1,0,0] neg_hi:[1,0,0]
	v_pk_mul_f32 v[98:99], v[92:93], v[98:99]
	v_pk_mul_f32 v[96:97], v[94:95], v[96:97]
	v_pk_mul_f32 v[102:103], v[88:89], v[102:103]
	v_pk_mul_f32 v[100:101], v[90:91], v[100:101]
	v_exp_f32_e32 v98, v98
	v_exp_f32_e32 v99, v99
	v_exp_f32_e32 v96, v96
	v_exp_f32_e32 v97, v97
	v_exp_f32_e32 v102, v102
	v_exp_f32_e32 v103, v103
	v_exp_f32_e32 v100, v100
	v_exp_f32_e32 v101, v101
	v_pk_add_f32 v[98:99], v[98:99], 1.0 op_sel_hi:[1,0]
	v_pk_add_f32 v[96:97], v[96:97], 1.0 op_sel_hi:[1,0]
	v_pk_add_f32 v[102:103], v[102:103], 1.0 op_sel_hi:[1,0]
	v_pk_add_f32 v[100:101], v[100:101], 1.0 op_sel_hi:[1,0]
	v_rcp_f32_e32 v98, v98
	v_rcp_f32_e32 v99, v99
	v_rcp_f32_e32 v96, v96
	v_rcp_f32_e32 v97, v97
	v_rcp_f32_e32 v102, v102
	v_rcp_f32_e32 v103, v103
	v_rcp_f32_e32 v100, v100
	v_rcp_f32_e32 v101, v101
	v_pk_mul_f32 v[92:93], v[92:93], v[98:99]
	v_pk_mul_f32 v[94:95], v[94:95], v[96:97]
	v_pk_mul_f32 v[96:97], v[88:89], v[102:103]
	v_pk_mul_f32 v[88:89], v[90:91], v[100:101]
	v_cvt_pk_f16_f32 v90, v96, v97
	v_cvt_pk_f16_f32 v91, v88, v89
	v_cvt_pk_f16_f32 v89, v94, v95
	v_cvt_pk_f16_f32 v88, v92, v93
	global_store_dwordx4 v[120:121], v[88:91], off offset:256 sc1
	v_pk_add_f32 v[86:87], v[86:87], v[14:15]
	v_pk_add_f32 v[84:85], v[84:85], v[12:13]
	v_pk_add_f32 v[82:83], v[82:83], v[10:11]
	v_pk_add_f32 v[80:81], v[80:81], v[8:9]
	v_pk_mul_f32 v[88:89], v[86:87], v[86:87]
	v_pk_mul_f32 v[90:91], v[84:85], v[84:85]
	v_pk_mul_f32 v[92:93], v[82:83], v[82:83]
	v_pk_mul_f32 v[94:95], v[80:81], v[80:81]
	v_pk_fma_f32 v[90:91], v[90:91], s[0:1], v[144:145] op_sel_hi:[1,0,0] neg_lo:[1,0,0] neg_hi:[1,0,0]
	v_pk_fma_f32 v[88:89], v[88:89], s[0:1], v[144:145] op_sel_hi:[1,0,0] neg_lo:[1,0,0] neg_hi:[1,0,0]
	v_pk_fma_f32 v[94:95], v[94:95], s[0:1], v[144:145] op_sel_hi:[1,0,0] neg_lo:[1,0,0] neg_hi:[1,0,0]
	v_pk_fma_f32 v[92:93], v[92:93], s[0:1], v[144:145] op_sel_hi:[1,0,0] neg_lo:[1,0,0] neg_hi:[1,0,0]
	v_pk_mul_f32 v[90:91], v[84:85], v[90:91]
	v_pk_mul_f32 v[88:89], v[86:87], v[88:89]
	v_pk_mul_f32 v[94:95], v[80:81], v[94:95]
	v_pk_mul_f32 v[92:93], v[82:83], v[92:93]
	v_exp_f32_e32 v90, v90
	v_exp_f32_e32 v91, v91
	v_exp_f32_e32 v88, v88
	v_exp_f32_e32 v89, v89
	v_exp_f32_e32 v94, v94
	v_exp_f32_e32 v95, v95
	v_exp_f32_e32 v92, v92
	v_exp_f32_e32 v93, v93
	v_pk_add_f32 v[90:91], v[90:91], 1.0 op_sel_hi:[1,0]
	v_pk_add_f32 v[88:89], v[88:89], 1.0 op_sel_hi:[1,0]
	v_pk_add_f32 v[94:95], v[94:95], 1.0 op_sel_hi:[1,0]
	v_pk_add_f32 v[92:93], v[92:93], 1.0 op_sel_hi:[1,0]
	v_rcp_f32_e32 v90, v90
	v_rcp_f32_e32 v91, v91
	v_rcp_f32_e32 v88, v88
	v_rcp_f32_e32 v89, v89
	v_rcp_f32_e32 v94, v94
	v_rcp_f32_e32 v95, v95
	v_rcp_f32_e32 v92, v92
	v_rcp_f32_e32 v93, v93
	v_pk_mul_f32 v[84:85], v[84:85], v[90:91]
	v_pk_mul_f32 v[86:87], v[86:87], v[88:89]
	v_pk_mul_f32 v[88:89], v[80:81], v[94:95]
	v_pk_mul_f32 v[80:81], v[82:83], v[92:93]
	v_cvt_pk_f16_f32 v82, v88, v89
	v_cvt_pk_f16_f32 v83, v80, v81
	v_cvt_pk_f16_f32 v81, v86, v87
	v_cvt_pk_f16_f32 v80, v84, v85
	global_store_dwordx4 v[112:113], v[80:83], off offset:256 sc1
	v_pk_add_f32 v[72:73], v[72:73], v[48:49]
	v_pk_add_f32 v[78:79], v[78:79], v[54:55]
	v_pk_add_f32 v[76:77], v[76:77], v[52:53]
	v_pk_add_f32 v[74:75], v[74:75], v[50:51]
	v_pk_mul_f32 v[88:89], v[72:73], v[72:73]
	v_pk_mul_f32 v[82:83], v[78:79], v[78:79]
	v_pk_mul_f32 v[84:85], v[76:77], v[76:77]
	v_pk_mul_f32 v[86:87], v[74:75], v[74:75]
	v_pk_fma_f32 v[88:89], v[88:89], s[0:1], v[144:145] op_sel_hi:[1,0,0] neg_lo:[1,0,0] neg_hi:[1,0,0]
	v_pk_fma_f32 v[84:85], v[84:85], s[0:1], v[144:145] op_sel_hi:[1,0,0] neg_lo:[1,0,0] neg_hi:[1,0,0]
	v_pk_fma_f32 v[82:83], v[82:83], s[0:1], v[144:145] op_sel_hi:[1,0,0] neg_lo:[1,0,0] neg_hi:[1,0,0]
	v_pk_mul_f32 v[88:89], v[72:73], v[88:89]
	v_pk_fma_f32 v[86:87], v[86:87], s[0:1], v[144:145] op_sel_hi:[1,0,0] neg_lo:[1,0,0] neg_hi:[1,0,0]
	v_pk_mul_f32 v[84:85], v[76:77], v[84:85]
	v_pk_mul_f32 v[82:83], v[78:79], v[82:83]
	v_exp_f32_e32 v88, v88
	v_exp_f32_e32 v89, v89
	v_pk_mul_f32 v[86:87], v[74:75], v[86:87]
	v_exp_f32_e32 v84, v84
	v_exp_f32_e32 v85, v85
	v_exp_f32_e32 v82, v82
	v_exp_f32_e32 v83, v83
	v_exp_f32_e32 v86, v86
	v_exp_f32_e32 v87, v87
	v_pk_add_f32 v[88:89], v[88:89], 1.0 op_sel_hi:[1,0]
	v_pk_add_f32 v[84:85], v[84:85], 1.0 op_sel_hi:[1,0]
	v_pk_add_f32 v[82:83], v[82:83], 1.0 op_sel_hi:[1,0]
	v_rcp_f32_e32 v88, v88
	v_rcp_f32_e32 v89, v89
	v_pk_add_f32 v[86:87], v[86:87], 1.0 op_sel_hi:[1,0]
	v_rcp_f32_e32 v84, v84
	v_rcp_f32_e32 v85, v85
	v_rcp_f32_e32 v82, v82
	v_rcp_f32_e32 v83, v83
	v_rcp_f32_e32 v86, v86
	v_rcp_f32_e32 v87, v87
	v_add_u32_e32 v80, s11, v166
	v_pk_mul_f32 v[72:73], v[72:73], v[88:89]
	v_ashrrev_i32_e32 v81, 31, v80
	v_pk_mul_f32 v[84:85], v[76:77], v[84:85]
	v_pk_mul_f32 v[78:79], v[78:79], v[82:83]
	v_pk_mul_f32 v[74:75], v[74:75], v[86:87]
	v_cvt_pk_f16_f32 v76, v72, v73
	v_lshlrev_b64 v[72:73], 14, v[80:81]
	v_cvt_pk_f16_f32 v77, v74, v75
	v_cvt_pk_f16_f32 v75, v78, v79
	v_cvt_pk_f16_f32 v74, v84, v85
	v_lshl_add_u64 v[72:73], v[146:147], 0, v[72:73]
	global_store_dwordx4 v[72:73], v[74:77], off sc1
	v_pk_add_f32 v[64:65], v[64:65], v[48:49]
	v_pk_add_f32 v[70:71], v[70:71], v[54:55]
	v_pk_add_f32 v[68:69], v[68:69], v[52:53]
	v_pk_add_f32 v[66:67], v[66:67], v[50:51]
	v_pk_mul_f32 v[84:85], v[64:65], v[64:65]
	v_pk_mul_f32 v[76:77], v[70:71], v[70:71]
	v_pk_mul_f32 v[78:79], v[68:69], v[68:69]
	v_pk_mul_f32 v[82:83], v[66:67], v[66:67]
	v_pk_fma_f32 v[84:85], v[84:85], s[0:1], v[144:145] op_sel_hi:[1,0,0] neg_lo:[1,0,0] neg_hi:[1,0,0]
	v_pk_fma_f32 v[78:79], v[78:79], s[0:1], v[144:145] op_sel_hi:[1,0,0] neg_lo:[1,0,0] neg_hi:[1,0,0]
	v_pk_fma_f32 v[76:77], v[76:77], s[0:1], v[144:145] op_sel_hi:[1,0,0] neg_lo:[1,0,0] neg_hi:[1,0,0]
	v_pk_mul_f32 v[84:85], v[64:65], v[84:85]
	v_pk_fma_f32 v[82:83], v[82:83], s[0:1], v[144:145] op_sel_hi:[1,0,0] neg_lo:[1,0,0] neg_hi:[1,0,0]
	v_pk_mul_f32 v[78:79], v[68:69], v[78:79]
	v_pk_mul_f32 v[76:77], v[70:71], v[76:77]
	v_exp_f32_e32 v84, v84
	v_exp_f32_e32 v85, v85
	v_pk_mul_f32 v[82:83], v[66:67], v[82:83]
	v_exp_f32_e32 v78, v78
	v_exp_f32_e32 v79, v79
	v_exp_f32_e32 v76, v76
	v_exp_f32_e32 v77, v77
	v_exp_f32_e32 v82, v82
	v_exp_f32_e32 v83, v83
	v_pk_add_f32 v[84:85], v[84:85], 1.0 op_sel_hi:[1,0]
	v_pk_add_f32 v[78:79], v[78:79], 1.0 op_sel_hi:[1,0]
	v_pk_add_f32 v[76:77], v[76:77], 1.0 op_sel_hi:[1,0]
	v_rcp_f32_e32 v84, v84
	v_rcp_f32_e32 v85, v85
	v_pk_add_f32 v[82:83], v[82:83], 1.0 op_sel_hi:[1,0]
	v_rcp_f32_e32 v78, v78
	v_rcp_f32_e32 v79, v79
	v_rcp_f32_e32 v76, v76
	v_rcp_f32_e32 v77, v77
	v_rcp_f32_e32 v82, v82
	v_rcp_f32_e32 v83, v83
	v_or_b32_e32 v74, 16, v80
	v_pk_mul_f32 v[64:65], v[64:65], v[84:85]
	v_ashrrev_i32_e32 v75, 31, v74
	v_pk_mul_f32 v[78:79], v[68:69], v[78:79]
	v_pk_mul_f32 v[70:71], v[70:71], v[76:77]
	v_pk_mul_f32 v[66:67], v[66:67], v[82:83]
	v_cvt_pk_f16_f32 v68, v64, v65
	v_lshlrev_b64 v[64:65], 14, v[74:75]
	v_cvt_pk_f16_f32 v69, v66, v67
	v_cvt_pk_f16_f32 v67, v70, v71
	v_cvt_pk_f16_f32 v66, v78, v79
	v_lshl_add_u64 v[64:65], v[146:147], 0, v[64:65]
	global_store_dwordx4 v[64:65], v[66:69], off sc1
	v_pk_add_f32 v[56:57], v[56:57], v[48:49]
	v_pk_add_f32 v[62:63], v[62:63], v[54:55]
	v_pk_add_f32 v[60:61], v[60:61], v[52:53]
	v_pk_add_f32 v[58:59], v[58:59], v[50:51]
	v_pk_mul_f32 v[76:77], v[56:57], v[56:57]
	v_pk_mul_f32 v[68:69], v[62:63], v[62:63]
	v_pk_mul_f32 v[70:71], v[60:61], v[60:61]
	v_pk_mul_f32 v[74:75], v[58:59], v[58:59]
	v_pk_fma_f32 v[76:77], v[76:77], s[0:1], v[144:145] op_sel_hi:[1,0,0] neg_lo:[1,0,0] neg_hi:[1,0,0]
	v_pk_fma_f32 v[70:71], v[70:71], s[0:1], v[144:145] op_sel_hi:[1,0,0] neg_lo:[1,0,0] neg_hi:[1,0,0]
	v_pk_fma_f32 v[68:69], v[68:69], s[0:1], v[144:145] op_sel_hi:[1,0,0] neg_lo:[1,0,0] neg_hi:[1,0,0]
	v_pk_mul_f32 v[76:77], v[56:57], v[76:77]
	v_pk_fma_f32 v[74:75], v[74:75], s[0:1], v[144:145] op_sel_hi:[1,0,0] neg_lo:[1,0,0] neg_hi:[1,0,0]
	v_pk_mul_f32 v[70:71], v[60:61], v[70:71]
	v_pk_mul_f32 v[68:69], v[62:63], v[68:69]
	v_exp_f32_e32 v76, v76
	v_exp_f32_e32 v77, v77
	v_pk_mul_f32 v[74:75], v[58:59], v[74:75]
	v_exp_f32_e32 v70, v70
	v_exp_f32_e32 v71, v71
	v_exp_f32_e32 v68, v68
	v_exp_f32_e32 v69, v69
	v_exp_f32_e32 v74, v74
	v_exp_f32_e32 v75, v75
	v_pk_add_f32 v[76:77], v[76:77], 1.0 op_sel_hi:[1,0]
	v_pk_add_f32 v[70:71], v[70:71], 1.0 op_sel_hi:[1,0]
	v_pk_add_f32 v[68:69], v[68:69], 1.0 op_sel_hi:[1,0]
	v_rcp_f32_e32 v76, v76
	v_rcp_f32_e32 v77, v77
	v_pk_add_f32 v[74:75], v[74:75], 1.0 op_sel_hi:[1,0]
	v_rcp_f32_e32 v70, v70
	v_rcp_f32_e32 v71, v71
	v_rcp_f32_e32 v68, v68
	v_rcp_f32_e32 v69, v69
	v_rcp_f32_e32 v74, v74
	v_rcp_f32_e32 v75, v75
	v_or_b32_e32 v66, 32, v80
	v_pk_mul_f32 v[56:57], v[56:57], v[76:77]
	v_ashrrev_i32_e32 v67, 31, v66
	v_pk_mul_f32 v[70:71], v[60:61], v[70:71]
	v_pk_mul_f32 v[62:63], v[62:63], v[68:69]
	v_pk_mul_f32 v[58:59], v[58:59], v[74:75]
	v_cvt_pk_f16_f32 v60, v56, v57
	v_lshlrev_b64 v[56:57], 14, v[66:67]
	v_cvt_pk_f16_f32 v61, v58, v59
	v_cvt_pk_f16_f32 v59, v62, v63
	v_cvt_pk_f16_f32 v58, v70, v71
	v_lshl_add_u64 v[56:57], v[146:147], 0, v[56:57]
	global_store_dwordx4 v[56:57], v[58:61], off sc1
	v_pk_add_f32 v[40:41], v[40:41], v[48:49]
	v_pk_add_f32 v[46:47], v[46:47], v[54:55]
	v_pk_add_f32 v[44:45], v[44:45], v[52:53]
	v_pk_add_f32 v[42:43], v[42:43], v[50:51]
	v_pk_mul_f32 v[54:55], v[40:41], v[40:41]
	v_pk_mul_f32 v[48:49], v[46:47], v[46:47]
	v_pk_mul_f32 v[50:51], v[44:45], v[44:45]
	v_pk_mul_f32 v[52:53], v[42:43], v[42:43]
	v_pk_fma_f32 v[54:55], v[54:55], s[0:1], v[144:145] op_sel_hi:[1,0,0] neg_lo:[1,0,0] neg_hi:[1,0,0]
	v_pk_fma_f32 v[50:51], v[50:51], s[0:1], v[144:145] op_sel_hi:[1,0,0] neg_lo:[1,0,0] neg_hi:[1,0,0]
	v_pk_fma_f32 v[48:49], v[48:49], s[0:1], v[144:145] op_sel_hi:[1,0,0] neg_lo:[1,0,0] neg_hi:[1,0,0]
	v_pk_mul_f32 v[54:55], v[40:41], v[54:55]
	v_pk_fma_f32 v[52:53], v[52:53], s[0:1], v[144:145] op_sel_hi:[1,0,0] neg_lo:[1,0,0] neg_hi:[1,0,0]
	v_pk_mul_f32 v[50:51], v[44:45], v[50:51]
	v_pk_mul_f32 v[48:49], v[46:47], v[48:49]
	v_exp_f32_e32 v54, v54
	v_exp_f32_e32 v55, v55
	v_pk_mul_f32 v[52:53], v[42:43], v[52:53]
	v_exp_f32_e32 v50, v50
	v_exp_f32_e32 v51, v51
	v_exp_f32_e32 v48, v48
	v_exp_f32_e32 v49, v49
	v_exp_f32_e32 v52, v52
	v_exp_f32_e32 v53, v53
	v_pk_add_f32 v[54:55], v[54:55], 1.0 op_sel_hi:[1,0]
	v_pk_add_f32 v[50:51], v[50:51], 1.0 op_sel_hi:[1,0]
	v_pk_add_f32 v[48:49], v[48:49], 1.0 op_sel_hi:[1,0]
	v_rcp_f32_e32 v54, v54
	v_rcp_f32_e32 v55, v55
	v_pk_add_f32 v[52:53], v[52:53], 1.0 op_sel_hi:[1,0]
	v_rcp_f32_e32 v50, v50
	v_rcp_f32_e32 v51, v51
	v_rcp_f32_e32 v48, v48
	v_rcp_f32_e32 v49, v49
	v_rcp_f32_e32 v52, v52
	v_rcp_f32_e32 v53, v53
	v_or_b32_e32 v58, 48, v80
	v_pk_mul_f32 v[40:41], v[40:41], v[54:55]
	v_ashrrev_i32_e32 v59, 31, v58
	v_pk_mul_f32 v[50:51], v[44:45], v[50:51]
	v_pk_mul_f32 v[46:47], v[46:47], v[48:49]
	v_pk_mul_f32 v[42:43], v[42:43], v[52:53]
	v_cvt_pk_f16_f32 v44, v40, v41
	v_lshlrev_b64 v[40:41], 14, v[58:59]
	v_cvt_pk_f16_f32 v45, v42, v43
	v_cvt_pk_f16_f32 v43, v46, v47
	v_cvt_pk_f16_f32 v42, v50, v51
	v_lshl_add_u64 v[40:41], v[146:147], 0, v[40:41]
	global_store_dwordx4 v[40:41], v[42:45], off sc1
	v_pk_add_f32 v[38:39], v[38:39], v[14:15]
	v_pk_add_f32 v[36:37], v[36:37], v[12:13]
	v_pk_add_f32 v[34:35], v[34:35], v[10:11]
	v_pk_add_f32 v[32:33], v[32:33], v[8:9]
	v_pk_mul_f32 v[42:43], v[38:39], v[38:39]
	v_pk_mul_f32 v[44:45], v[36:37], v[36:37]
	v_pk_mul_f32 v[46:47], v[34:35], v[34:35]
	v_pk_mul_f32 v[48:49], v[32:33], v[32:33]
	v_pk_fma_f32 v[44:45], v[44:45], s[0:1], v[144:145] op_sel_hi:[1,0,0] neg_lo:[1,0,0] neg_hi:[1,0,0]
	v_pk_fma_f32 v[42:43], v[42:43], s[0:1], v[144:145] op_sel_hi:[1,0,0] neg_lo:[1,0,0] neg_hi:[1,0,0]
	v_pk_fma_f32 v[48:49], v[48:49], s[0:1], v[144:145] op_sel_hi:[1,0,0] neg_lo:[1,0,0] neg_hi:[1,0,0]
	v_pk_fma_f32 v[46:47], v[46:47], s[0:1], v[144:145] op_sel_hi:[1,0,0] neg_lo:[1,0,0] neg_hi:[1,0,0]
	v_pk_mul_f32 v[44:45], v[36:37], v[44:45]
	v_pk_mul_f32 v[42:43], v[38:39], v[42:43]
	v_pk_mul_f32 v[48:49], v[32:33], v[48:49]
	v_pk_mul_f32 v[46:47], v[34:35], v[46:47]
	v_exp_f32_e32 v44, v44
	v_exp_f32_e32 v45, v45
	v_exp_f32_e32 v42, v42
	v_exp_f32_e32 v43, v43
	v_exp_f32_e32 v48, v48
	v_exp_f32_e32 v49, v49
	v_exp_f32_e32 v46, v46
	v_exp_f32_e32 v47, v47
	v_pk_add_f32 v[44:45], v[44:45], 1.0 op_sel_hi:[1,0]
	v_pk_add_f32 v[42:43], v[42:43], 1.0 op_sel_hi:[1,0]
	v_pk_add_f32 v[48:49], v[48:49], 1.0 op_sel_hi:[1,0]
	v_pk_add_f32 v[46:47], v[46:47], 1.0 op_sel_hi:[1,0]
	v_rcp_f32_e32 v44, v44
	v_rcp_f32_e32 v45, v45
	v_rcp_f32_e32 v42, v42
	v_rcp_f32_e32 v43, v43
	v_rcp_f32_e32 v48, v48
	v_rcp_f32_e32 v49, v49
	v_rcp_f32_e32 v46, v46
	v_rcp_f32_e32 v47, v47
	v_pk_mul_f32 v[36:37], v[36:37], v[44:45]
	v_pk_mul_f32 v[38:39], v[38:39], v[42:43]
	v_pk_mul_f32 v[42:43], v[32:33], v[48:49]
	v_pk_mul_f32 v[32:33], v[34:35], v[46:47]
	v_cvt_pk_f16_f32 v34, v42, v43
	v_cvt_pk_f16_f32 v35, v32, v33
	v_cvt_pk_f16_f32 v33, v38, v39
	v_cvt_pk_f16_f32 v32, v36, v37
	global_store_dwordx4 v[72:73], v[32:35], off offset:256 sc1
	v_pk_add_f32 v[30:31], v[30:31], v[14:15]
	v_pk_add_f32 v[28:29], v[28:29], v[12:13]
	v_pk_add_f32 v[26:27], v[26:27], v[10:11]
	v_pk_add_f32 v[24:25], v[24:25], v[8:9]
	v_pk_mul_f32 v[32:33], v[30:31], v[30:31]
	v_pk_mul_f32 v[34:35], v[28:29], v[28:29]
	v_pk_mul_f32 v[36:37], v[26:27], v[26:27]
	v_pk_mul_f32 v[38:39], v[24:25], v[24:25]
	v_pk_fma_f32 v[34:35], v[34:35], s[0:1], v[144:145] op_sel_hi:[1,0,0] neg_lo:[1,0,0] neg_hi:[1,0,0]
	v_pk_fma_f32 v[32:33], v[32:33], s[0:1], v[144:145] op_sel_hi:[1,0,0] neg_lo:[1,0,0] neg_hi:[1,0,0]
	v_pk_fma_f32 v[38:39], v[38:39], s[0:1], v[144:145] op_sel_hi:[1,0,0] neg_lo:[1,0,0] neg_hi:[1,0,0]
	v_pk_fma_f32 v[36:37], v[36:37], s[0:1], v[144:145] op_sel_hi:[1,0,0] neg_lo:[1,0,0] neg_hi:[1,0,0]
	v_pk_mul_f32 v[34:35], v[28:29], v[34:35]
	v_pk_mul_f32 v[32:33], v[30:31], v[32:33]
	v_pk_mul_f32 v[38:39], v[24:25], v[38:39]
	v_pk_mul_f32 v[36:37], v[26:27], v[36:37]
	v_exp_f32_e32 v34, v34
	v_exp_f32_e32 v35, v35
	v_exp_f32_e32 v32, v32
	v_exp_f32_e32 v33, v33
	v_exp_f32_e32 v38, v38
	v_exp_f32_e32 v39, v39
	v_exp_f32_e32 v36, v36
	v_exp_f32_e32 v37, v37
	v_pk_add_f32 v[34:35], v[34:35], 1.0 op_sel_hi:[1,0]
	v_pk_add_f32 v[32:33], v[32:33], 1.0 op_sel_hi:[1,0]
	v_pk_add_f32 v[38:39], v[38:39], 1.0 op_sel_hi:[1,0]
	v_pk_add_f32 v[36:37], v[36:37], 1.0 op_sel_hi:[1,0]
	v_rcp_f32_e32 v34, v34
	v_rcp_f32_e32 v35, v35
	v_rcp_f32_e32 v32, v32
	v_rcp_f32_e32 v33, v33
	v_rcp_f32_e32 v38, v38
	v_rcp_f32_e32 v39, v39
	v_rcp_f32_e32 v36, v36
	v_rcp_f32_e32 v37, v37
	v_pk_mul_f32 v[28:29], v[28:29], v[34:35]
	v_pk_mul_f32 v[30:31], v[30:31], v[32:33]
	v_pk_mul_f32 v[32:33], v[24:25], v[38:39]
	v_pk_mul_f32 v[24:25], v[26:27], v[36:37]
	v_cvt_pk_f16_f32 v26, v32, v33
	v_cvt_pk_f16_f32 v27, v24, v25
	v_cvt_pk_f16_f32 v25, v30, v31
	v_cvt_pk_f16_f32 v24, v28, v29
	global_store_dwordx4 v[64:65], v[24:27], off offset:256 sc1
	v_pk_add_f32 v[22:23], v[22:23], v[14:15]
	v_pk_add_f32 v[20:21], v[20:21], v[12:13]
	v_pk_add_f32 v[18:19], v[18:19], v[10:11]
	v_pk_add_f32 v[16:17], v[16:17], v[8:9]
	v_pk_mul_f32 v[24:25], v[22:23], v[22:23]
	v_pk_mul_f32 v[26:27], v[20:21], v[20:21]
	v_pk_mul_f32 v[28:29], v[18:19], v[18:19]
	v_pk_mul_f32 v[30:31], v[16:17], v[16:17]
	v_pk_fma_f32 v[26:27], v[26:27], s[0:1], v[144:145] op_sel_hi:[1,0,0] neg_lo:[1,0,0] neg_hi:[1,0,0]
	v_pk_fma_f32 v[24:25], v[24:25], s[0:1], v[144:145] op_sel_hi:[1,0,0] neg_lo:[1,0,0] neg_hi:[1,0,0]
	v_pk_fma_f32 v[30:31], v[30:31], s[0:1], v[144:145] op_sel_hi:[1,0,0] neg_lo:[1,0,0] neg_hi:[1,0,0]
	v_pk_fma_f32 v[28:29], v[28:29], s[0:1], v[144:145] op_sel_hi:[1,0,0] neg_lo:[1,0,0] neg_hi:[1,0,0]
	v_pk_mul_f32 v[26:27], v[20:21], v[26:27]
	v_pk_mul_f32 v[24:25], v[22:23], v[24:25]
	v_pk_mul_f32 v[30:31], v[16:17], v[30:31]
	v_pk_mul_f32 v[28:29], v[18:19], v[28:29]
	v_exp_f32_e32 v26, v26
	v_exp_f32_e32 v27, v27
	v_exp_f32_e32 v24, v24
	v_exp_f32_e32 v25, v25
	v_exp_f32_e32 v30, v30
	v_exp_f32_e32 v31, v31
	v_exp_f32_e32 v28, v28
	v_exp_f32_e32 v29, v29
	v_pk_add_f32 v[26:27], v[26:27], 1.0 op_sel_hi:[1,0]
	v_pk_add_f32 v[24:25], v[24:25], 1.0 op_sel_hi:[1,0]
	v_pk_add_f32 v[30:31], v[30:31], 1.0 op_sel_hi:[1,0]
	v_pk_add_f32 v[28:29], v[28:29], 1.0 op_sel_hi:[1,0]
	v_rcp_f32_e32 v26, v26
	v_rcp_f32_e32 v27, v27
	v_rcp_f32_e32 v24, v24
	v_rcp_f32_e32 v25, v25
	v_rcp_f32_e32 v30, v30
	v_rcp_f32_e32 v31, v31
	v_rcp_f32_e32 v28, v28
	v_rcp_f32_e32 v29, v29
	v_pk_mul_f32 v[20:21], v[20:21], v[26:27]
	v_pk_mul_f32 v[22:23], v[22:23], v[24:25]
	v_pk_mul_f32 v[24:25], v[16:17], v[30:31]
	v_pk_mul_f32 v[16:17], v[18:19], v[28:29]
	v_cvt_pk_f16_f32 v18, v24, v25
	v_cvt_pk_f16_f32 v19, v16, v17
	v_cvt_pk_f16_f32 v17, v22, v23
	v_cvt_pk_f16_f32 v16, v20, v21
	global_store_dwordx4 v[56:57], v[16:19], off offset:256 sc1
	v_pk_add_f32 v[6:7], v[6:7], v[14:15]
	v_pk_add_f32 v[4:5], v[4:5], v[12:13]
	v_pk_add_f32 v[2:3], v[2:3], v[10:11]
	v_pk_add_f32 v[0:1], v[0:1], v[8:9]
	v_pk_mul_f32 v[8:9], v[6:7], v[6:7]
	v_pk_mul_f32 v[10:11], v[4:5], v[4:5]
	v_pk_mul_f32 v[12:13], v[2:3], v[2:3]
	v_pk_mul_f32 v[14:15], v[0:1], v[0:1]
	v_pk_fma_f32 v[10:11], v[10:11], s[0:1], v[144:145] op_sel_hi:[1,0,0] neg_lo:[1,0,0] neg_hi:[1,0,0]
	v_pk_fma_f32 v[8:9], v[8:9], s[0:1], v[144:145] op_sel_hi:[1,0,0] neg_lo:[1,0,0] neg_hi:[1,0,0]
	v_pk_fma_f32 v[14:15], v[14:15], s[0:1], v[144:145] op_sel_hi:[1,0,0] neg_lo:[1,0,0] neg_hi:[1,0,0]
	v_pk_fma_f32 v[12:13], v[12:13], s[0:1], v[144:145] op_sel_hi:[1,0,0] neg_lo:[1,0,0] neg_hi:[1,0,0]
	v_pk_mul_f32 v[10:11], v[4:5], v[10:11]
	v_pk_mul_f32 v[8:9], v[6:7], v[8:9]
	v_pk_mul_f32 v[14:15], v[0:1], v[14:15]
	v_pk_mul_f32 v[12:13], v[2:3], v[12:13]
	v_exp_f32_e32 v10, v10
	v_exp_f32_e32 v11, v11
	v_exp_f32_e32 v8, v8
	v_exp_f32_e32 v9, v9
	v_exp_f32_e32 v14, v14
	v_exp_f32_e32 v15, v15
	v_exp_f32_e32 v12, v12
	v_exp_f32_e32 v13, v13
	v_pk_add_f32 v[10:11], v[10:11], 1.0 op_sel_hi:[1,0]
	v_pk_add_f32 v[8:9], v[8:9], 1.0 op_sel_hi:[1,0]
	v_pk_add_f32 v[14:15], v[14:15], 1.0 op_sel_hi:[1,0]
	v_pk_add_f32 v[12:13], v[12:13], 1.0 op_sel_hi:[1,0]
	v_rcp_f32_e32 v10, v10
	v_rcp_f32_e32 v11, v11
	v_rcp_f32_e32 v8, v8
	v_rcp_f32_e32 v9, v9
	v_rcp_f32_e32 v14, v14
	v_rcp_f32_e32 v15, v15
	v_rcp_f32_e32 v12, v12
	v_rcp_f32_e32 v13, v13
	v_pk_mul_f32 v[4:5], v[4:5], v[10:11]
	v_pk_mul_f32 v[6:7], v[6:7], v[8:9]
	v_pk_mul_f32 v[8:9], v[0:1], v[14:15]
	v_pk_mul_f32 v[0:1], v[2:3], v[12:13]
	v_cvt_pk_f16_f32 v2, v8, v9
	v_cvt_pk_f16_f32 v3, v0, v1
	v_cvt_pk_f16_f32 v1, v6, v7
	v_cvt_pk_f16_f32 v0, v4, v5
	global_store_dwordx4 v[40:41], v[0:3], off offset:256 sc1
	s_endpgm
	.p2align	8
